# ssd_out: 12 stage-1 tile loads issued at the item top under the dt latency (own registers, copied after the barrier)
# speedup vs baseline: 1.0029x; 1.0029x over previous
.LBB0_641:
	s_and_b32 s21, s91, 0x1ff
	s_lshl_b32 s20, s21, 6
	v_add_u32_e32 v201, s20, v132
	v_lshlrev_b32_e32 v0, 5, v201
	global_load_dword v0, v0, s[18:19]
	s_nop 0
	global_load_dword v1, v209, s[6:7]
	global_load_dword v2, v209, s[8:9]
	s_mov_b32 s12, 0xbfb8aa3b
	v_add_u32_e32 v3, s20, v141
	v_add_u32_e32 v4, s20, v142
	v_add_u32_e32 v5, s20, v143
	v_add_u32_e32 v6, s20, v144
	v_add_u32_e32 v8, s20, v145
	v_add_u32_e32 v10, s20, v146
	v_add_u32_e32 v12, s20, v147
	v_add_u32_e32 v14, s20, v148
	v_add_u32_e32 v16, s20, v149
	v_add_u32_e32 v17, s20, v150
	v_add_u32_e32 v18, s20, v151
	v_add_u32_e32 v19, s20, v152
	v_mad_i64_i32 v[56:57], s[98:99], v3, s33, v[104:105]
	v_mad_i64_i32 v[60:61], s[98:99], v4, s33, v[106:107]
	v_mad_i64_i32 v[64:65], s[98:99], v5, s33, v[108:109]
	v_mad_i64_i32 v[68:69], s[98:99], v6, s33, v[110:111]
	v_mad_i64_i32 v[72:73], s[98:99], v8, s33, v[112:113]
	v_mad_i64_i32 v[76:77], s[98:99], v10, s33, v[114:115]
	v_mad_i64_i32 v[80:81], s[98:99], v12, s33, v[116:117]
	v_mad_i64_i32 v[84:85], s[98:99], v14, s33, v[118:119]
	v_mad_i64_i32 v[88:89], s[98:99], v16, s33, v[120:121]
	v_mad_i64_i32 v[92:93], s[98:99], v17, s33, v[122:123]
	v_mad_i64_i32 v[96:97], s[98:99], v18, s33, v[124:125]
	v_mad_i64_i32 v[100:101], s[98:99], v19, s33, v[126:127]
	global_load_dwordx4 v[56:59], v[56:57], off
	global_load_dwordx4 v[60:63], v[60:61], off
	global_load_dwordx4 v[64:67], v[64:65], off
	global_load_dwordx4 v[68:71], v[68:69], off
	global_load_dwordx4 v[72:75], v[72:73], off
	global_load_dwordx4 v[76:79], v[76:77], off
	global_load_dwordx4 v[80:83], v[80:81], off
	global_load_dwordx4 v[84:87], v[84:85], off
	global_load_dwordx4 v[88:91], v[88:89], off
	global_load_dwordx4 v[92:95], v[92:93], off
	global_load_dwordx4 v[96:99], v[96:97], off
	global_load_dwordx4 v[100:103], v[100:101], off
	s_waitcnt vmcnt(13)
	v_add_f32_e32 v0, v0, v1
	v_mul_f32_e64 v1, |v0|, s12
	v_exp_f32_e32 v7, v1
	s_waitcnt vmcnt(12)
	s_load_dwordx2 s[98:99], s[92:93], 0x80
	s_waitcnt lgkmcnt(0)
	s_add_u32 s98, s98, s4
	s_addc_u32 s99, s99, s5
	global_load_dword v231, v209, s[98:99]
	v_mul_f32_e32 v1, 0x3fb8aa3b, v2
	v_exp_f32_e32 v9, v1
	v_max_f32_e32 v2, 0, v0
	v_add_f32_e32 v11, 1.0, v7
	v_add_f32_e32 v13, -1.0, v11
	v_frexp_mant_f32_e32 v15, v11
	v_cvt_f64_f32_e32 v[0:1], v11
	s_mov_b32 s12, 0x3f2aaaab
	v_sub_f32_e32 v20, v13, v11
	v_frexp_exp_i32_f64_e32 v0, v[0:1]
	v_cmp_gt_f32_e32 vcc, s12, v15
	v_sub_f32_e32 v13, v7, v13
	v_add_f32_e32 v1, 1.0, v20
	v_subbrev_co_u32_e32 v0, vcc, 0, v0, vcc
	v_add_f32_e32 v1, v13, v1
	v_sub_u32_e32 v13, 0, v0
	v_cvt_f32_i32_e32 v0, v0
	v_ldexp_f32 v11, v11, v13
	v_ldexp_f32 v1, v1, v13
	v_add_f32_e32 v13, -1.0, v11
	v_add_f32_e32 v15, 1.0, v11
	v_add_f32_e32 v20, 1.0, v13
	v_add_f32_e32 v21, -1.0, v15
	v_sub_f32_e32 v20, v11, v20
	v_sub_f32_e32 v11, v11, v21
	v_mul_f32_e32 v21, 0x3f317218, v0
	v_add_f32_e32 v20, v1, v20
	v_add_f32_e32 v1, v1, v11
	s_mov_b32 s12, 0x3f317218
	v_fma_f32 v11, v0, s12, -v21
	v_add_f32_e32 v22, v13, v20
	v_add_f32_e32 v23, v15, v1
	v_fmac_f32_e32 v11, 0xb102e308, v0
	v_sub_f32_e32 v0, v22, v13
	v_sub_f32_e32 v13, v23, v15
	v_rcp_f32_e32 v15, v23
	v_add_f32_e32 v24, v21, v11
	v_sub_f32_e32 v1, v1, v13
	v_sub_f32_e32 v13, v24, v21
	v_sub_f32_e32 v11, v11, v13
	v_mul_f32_e32 v13, v22, v15
	v_sub_f32_e32 v0, v20, v0
	v_mul_f32_e32 v20, v23, v13
	v_fma_f32 v21, v13, v23, -v20
	v_fmac_f32_e32 v21, v13, v1
	v_add_f32_e32 v25, v20, v21
	v_sub_f32_e32 v26, v22, v25
	v_sub_f32_e32 v20, v25, v20
	v_sub_f32_e32 v22, v22, v26
	v_sub_f32_e32 v20, v20, v21
	v_sub_f32_e32 v21, v22, v25
	v_add_f32_e32 v0, v0, v21
	v_add_f32_e32 v0, v20, v0
	v_add_f32_e32 v20, v26, v0
	v_mul_f32_e32 v21, v15, v20
	v_sub_f32_e32 v22, v26, v20
	v_mul_f32_e32 v25, v23, v21
	v_add_f32_e32 v0, v0, v22
	v_add_f32_e32 v22, v13, v21
	v_fma_f32 v23, v21, v23, -v25
	v_sub_f32_e32 v13, v22, v13
	v_fmac_f32_e32 v23, v21, v1
	v_sub_f32_e32 v1, v21, v13
	v_add_f32_e32 v13, v25, v23
	v_sub_f32_e32 v21, v13, v25
	v_sub_f32_e32 v25, v20, v13
	v_sub_f32_e32 v20, v20, v25
	v_sub_f32_e32 v13, v20, v13
	v_sub_f32_e32 v21, v21, v23
	v_add_f32_e32 v0, v0, v13
	v_add_f32_e32 v0, v21, v0
	v_add_f32_e32 v0, v25, v0
	v_mul_f32_e32 v0, v15, v0
	v_add_f32_e32 v0, v1, v0
	v_add_f32_e32 v1, v22, v0
	v_mul_f32_e32 v13, v1, v1
	v_fmamk_f32 v21, v13, 0x3e9b6dac, v250
	v_sub_f32_e32 v15, v1, v22
	v_ldexp_f32 v20, v1, 1
	v_mul_f32_e32 v1, v1, v13
	v_fmaak_f32 v13, v13, v21, 0x3f2aaada
	v_mul_f32_e32 v1, v1, v13
	v_add_f32_e32 v13, v20, v1
	v_sub_f32_e32 v0, v0, v15
	v_sub_f32_e32 v15, v13, v20
	v_ldexp_f32 v0, v0, 1
	v_sub_f32_e32 v1, v1, v15
	v_add_f32_e32 v0, v0, v1
	v_add_f32_e32 v1, v13, v0
	v_sub_f32_e32 v13, v1, v13
	v_add_f32_e32 v15, v24, v1
	v_sub_f32_e32 v0, v0, v13
	v_sub_f32_e32 v13, v15, v24
	v_sub_f32_e32 v20, v15, v13
	v_sub_f32_e32 v1, v1, v13
	v_add_f32_e32 v13, v11, v0
	v_sub_f32_e32 v20, v24, v20
	v_sub_f32_e32 v21, v13, v11
	v_add_f32_e32 v1, v1, v20
	v_sub_f32_e32 v20, v13, v21
	v_sub_f32_e32 v0, v0, v21
	v_sub_f32_e32 v11, v11, v20
	v_add_f32_e32 v1, v13, v1
	v_add_f32_e32 v0, v0, v11
	v_add_f32_e32 v11, v15, v1
	v_sub_f32_e32 v13, v11, v15
	v_sub_f32_e32 v1, v1, v13
	v_add_f32_e32 v0, v0, v1
	s_mov_b32 s12, 0x7f800000
	v_add_f32_e32 v0, v11, v0
	v_cmp_neq_f32_e32 vcc, s12, v7
	v_mov_b32_e32 v1, 0x7fc00000
	s_mov_b32 s12, 0x33800000
	v_cndmask_b32_e32 v0, v251, v0, vcc
	v_cmp_ngt_f32_e32 vcc, -1.0, v7
	s_nop 1
	v_cndmask_b32_e32 v0, v1, v0, vcc
	v_cmp_neq_f32_e32 vcc, -1.0, v7
	s_nop 1
	v_cndmask_b32_e32 v0, v230, v0, vcc
	v_cmp_lt_f32_e64 vcc, |v7|, s12
	s_nop 1
	v_cndmask_b32_e32 v0, v0, v7, vcc
	v_add_f32_e32 v20, v2, v0
	v_mul_f32_e64 v7, v20, -v9
	ds_bpermute_b32 v11, v134, v7
	v_mad_i64_i32 v[0:1], s[12:13], v3, s33, v[104:105]
	v_mad_i64_i32 v[2:3], s[12:13], v4, s33, v[106:107]
	v_readlane_b32 s12, v253, 43
	s_waitcnt lgkmcnt(0)
	v_fma_f32 v4, v20, -v9, v11
	v_readlane_b32 s13, v253, 44
	s_nop 1
	v_cndmask_b32_e64 v9, v4, v7, s[12:13]
	ds_bpermute_b32 v11, v135, v9
	v_mad_i64_i32 v[4:5], s[12:13], v5, s33, v[108:109]
	v_mad_i64_i32 v[6:7], s[12:13], v6, s33, v[110:111]
	v_readlane_b32 s12, v253, 47
	s_waitcnt lgkmcnt(0)
	v_add_f32_e32 v11, v9, v11
	v_readlane_b32 s13, v253, 48
	s_nop 1
	v_cndmask_b32_e64 v13, v11, v9, s[12:13]
	ds_bpermute_b32 v15, v136, v13
	v_mad_i64_i32 v[8:9], s[12:13], v8, s33, v[112:113]
	v_mad_i64_i32 v[10:11], s[12:13], v10, s33, v[114:115]
	v_readlane_b32 s12, v253, 49
	s_waitcnt lgkmcnt(0)
	v_add_f32_e32 v15, v13, v15
	v_readlane_b32 s13, v253, 50
	s_nop 1
	v_cndmask_b32_e64 v21, v15, v13, s[12:13]
	ds_bpermute_b32 v22, v137, v21
	v_mad_i64_i32 v[12:13], s[12:13], v12, s33, v[116:117]
	v_mad_i64_i32 v[14:15], s[12:13], v14, s33, v[118:119]
	v_readlane_b32 s12, v253, 45
	s_waitcnt lgkmcnt(0)
	v_add_f32_e32 v22, v21, v22
	v_readlane_b32 s13, v253, 46
	s_nop 1
	v_cndmask_b32_e64 v21, v22, v21, s[12:13]
	ds_bpermute_b32 v22, v138, v21
	v_mad_i64_i32 v[48:49], s[12:13], v16, s33, v[120:121]
	v_mad_i64_i32 v[50:51], s[12:13], v17, s33, v[122:123]
	v_readlane_b32 s12, v253, 51
	s_waitcnt lgkmcnt(0)
	v_add_f32_e32 v16, v21, v22
	v_readlane_b32 s13, v253, 52
	s_nop 1
	v_cndmask_b32_e64 v16, v16, v21, s[12:13]
	ds_bpermute_b32 v17, v139, v16
	v_mad_i64_i32 v[52:53], s[12:13], v18, s33, v[124:125]
	v_mad_i64_i32 v[54:55], s[12:13], v19, s33, v[126:127]
	v_readlane_b32 s12, v253, 55
	s_waitcnt lgkmcnt(0)
	v_add_f32_e32 v17, v16, v17
	v_readlane_b32 s13, v253, 56
	s_nop 1
	v_cndmask_b32_e64 v16, v17, v16, s[12:13]
	ds_write2st64_b32 v140, v16, v20 offset1:8
	s_waitcnt lgkmcnt(0)
	s_barrier
	s_waitcnt vmcnt(0)
	v_mov_b64_e32 v[44:45], v[56:57]
	v_mov_b64_e32 v[46:47], v[58:59]
	v_mov_b64_e32 v[40:41], v[60:61]
	v_mov_b64_e32 v[42:43], v[62:63]
	v_mov_b64_e32 v[36:37], v[64:65]
	v_mov_b64_e32 v[38:39], v[66:67]
	v_mov_b64_e32 v[32:33], v[68:69]
	v_mov_b64_e32 v[34:35], v[70:71]
	v_mov_b64_e32 v[28:29], v[72:73]
	v_mov_b64_e32 v[30:31], v[74:75]
	v_mov_b64_e32 v[24:25], v[76:77]
	v_mov_b64_e32 v[26:27], v[78:79]
	v_mov_b64_e32 v[20:21], v[80:81]
	v_mov_b64_e32 v[22:23], v[82:83]
	v_mov_b64_e32 v[16:17], v[84:85]
	v_mov_b64_e32 v[18:19], v[86:87]
	v_mov_b64_e32 v[12:13], v[88:89]
	v_mov_b64_e32 v[14:15], v[90:91]
	v_mov_b64_e32 v[8:9], v[92:93]
	v_mov_b64_e32 v[10:11], v[94:95]
	v_mov_b64_e32 v[4:5], v[96:97]
	v_mov_b64_e32 v[6:7], v[98:99]
	v_mov_b64_e32 v[0:1], v[100:101]
	v_mov_b64_e32 v[2:3], v[102:103]
	s_mov_b64 s[12:13], exec
	v_readlane_b32 s76, v253, 59
	v_readlane_b32 s77, v253, 60
	s_and_b64 s[76:77], s[12:13], s[76:77]
	s_xor_b64 vcc, s[76:77], s[12:13]
	s_mov_b64 exec, s[76:77]
	s_cbranch_execz .LBB0_647
	s_mov_b64 s[12:13], exec
	v_readlane_b32 s76, v253, 61
	v_readlane_b32 s77, v253, 62
	s_and_b64 s[76:77], s[12:13], s[76:77]
	s_xor_b64 s[12:13], s[76:77], s[12:13]
	s_mov_b64 exec, s[76:77]
	s_cbranch_execz .LBB0_644
	s_waitcnt vmcnt(11)
	ds_write_b128 v157, v[44:47] offset:22528
